# attention row max / row sum lane exchanges via v_permlane16/32_swap instead of ds_bpermute round trips
# baseline (speedup 1.0000x reference)
.LBB0_389:
	s_add_i32 s87, s88, 0
	v_add3_u32 v13, s87, v129, v140
	v_add3_u32 v12, s87, v130, v140
	ds_read_b128 v[162:165], v13
	ds_read_b128 v[166:169], v12
	v_mov_b64_e32 v[92:93], s[38:39]
	v_mov_b64_e32 v[90:91], s[36:37]
	v_add3_u32 v13, s87, v129, v141
	s_waitcnt vmcnt(8) lgkmcnt(0)
	s_nop 1
	v_mfma_f32_16x16x128_f8f6f4 v[90:93], v[162:169], v[2:9], v[90:93]
	v_add3_u32 v12, s87, v130, v141
	ds_read_b128 v[162:165], v13
	ds_read_b128 v[166:169], v12
	v_mov_b64_e32 v[72:73], s[38:39]
	v_mov_b64_e32 v[70:71], s[36:37]
	s_waitcnt lgkmcnt(0)
	s_nop 1
	v_mfma_f32_16x16x128_f8f6f4 v[70:73], v[162:169], v[2:9], v[70:73]
	s_nop 11
	v_cndmask_b32_e64 v2, v112, v113, s[16:17]
	ds_read_b128 v[2:5], v2
	s_mov_b32 s16, 0xff800000
	v_cndmask_b32_e64 v13, v143, v113, s[20:21]
	s_waitcnt lgkmcnt(0)
	v_fmamk_f32 v2, v66, 0x3a0293ee, v2
	v_fmamk_f32 v3, v67, 0x3a0293ee, v3
	v_max3_f32 v6, v2, s16, v3
	v_fmamk_f32 v4, v68, 0x3a0293ee, v4
	v_fmac_f32_e32 v5, 0x3a0293ee, v69
	v_max3_f32 v12, v6, v4, v5
	v_cndmask_b32_e64 v6, v142, v113, s[18:19]
	ds_read_b128 v[6:9], v6
	s_waitcnt lgkmcnt(0)
	v_fmamk_f32 v6, v54, 0x3a0293ee, v6
	v_fmamk_f32 v7, v55, 0x3a0293ee, v7
	v_fmamk_f32 v8, v56, 0x3a0293ee, v8
	v_fmac_f32_e32 v9, 0x3a0293ee, v57
	ds_read_b128 v[54:57], v13
	v_max3_f32 v12, v12, v6, v7
	v_max3_f32 v12, v12, v8, v9
	s_waitcnt lgkmcnt(0)
	v_fmamk_f32 v13, v78, 0x3a0293ee, v54
	v_fmamk_f32 v54, v79, 0x3a0293ee, v55
	v_fmamk_f32 v55, v80, 0x3a0293ee, v56
	v_cndmask_b32_e64 v56, v144, v113, s[22:23]
	ds_read_b128 v[66:69], v56
	v_fmac_f32_e32 v57, 0x3a0293ee, v81
	v_max3_f32 v12, v12, v13, v54
	v_max3_f32 v12, v12, v55, v57
	s_waitcnt lgkmcnt(0)
	v_fmamk_f32 v56, v58, 0x3a0293ee, v66
	v_fmamk_f32 v66, v59, 0x3a0293ee, v67
	v_fmamk_f32 v67, v60, 0x3a0293ee, v68
	v_cndmask_b32_e64 v58, v145, v113, s[24:25]
	v_cndmask_b32_e64 v68, v146, v113, s[26:27]
	v_fmac_f32_e32 v69, 0x3a0293ee, v61
	ds_read_b128 v[58:61], v58
	ds_read_b128 v[78:81], v68
	v_max3_f32 v12, v12, v56, v66
	v_max3_f32 v12, v12, v67, v69
	s_waitcnt lgkmcnt(1)
	v_fmamk_f32 v58, v82, 0x3a0293ee, v58
	v_fmamk_f32 v59, v83, 0x3a0293ee, v59
	v_fmamk_f32 v60, v84, 0x3a0293ee, v60
	v_fmac_f32_e32 v61, 0x3a0293ee, v85
	s_waitcnt lgkmcnt(0)
	v_fmamk_f32 v68, v62, 0x3a0293ee, v78
	v_cndmask_b32_e64 v62, v147, v113, s[28:29]
	ds_read_b128 v[82:85], v10
	v_fmamk_f32 v79, v63, 0x3a0293ee, v79
	v_fmamk_f32 v80, v64, 0x3a0293ee, v80
	v_fmac_f32_e32 v81, 0x3a0293ee, v65
	ds_read_b128 v[62:65], v62
	v_max3_f32 v12, v12, v58, v59
	v_max3_f32 v12, v12, v60, v61
	v_max3_f32 v12, v12, v68, v79
	s_waitcnt lgkmcnt(1)
	v_fmamk_f32 v10, v74, 0x3a0293ee, v82
	v_fmamk_f32 v82, v75, 0x3a0293ee, v83
	v_fmamk_f32 v83, v76, 0x3a0293ee, v84
	v_fmac_f32_e32 v85, 0x3a0293ee, v77
	ds_read_b128 v[74:77], v111 offset:640
	v_max3_f32 v12, v12, v80, v81
	s_waitcnt lgkmcnt(1)
	v_fmamk_f32 v62, v86, 0x3a0293ee, v62
	v_fmamk_f32 v63, v87, 0x3a0293ee, v63
	v_fmamk_f32 v64, v88, 0x3a0293ee, v64
	v_fmac_f32_e32 v65, 0x3a0293ee, v89
	ds_read_b128 v[86:89], v111 offset:704
	v_max3_f32 v12, v12, v62, v63
	v_max3_f32 v12, v12, v64, v65
	v_max3_f32 v12, v12, v10, v82
	v_max3_f32 v12, v12, v83, v85
	s_waitcnt lgkmcnt(1)
	v_fmamk_f32 v74, v90, 0x3a0293ee, v74
	v_fmamk_f32 v75, v91, 0x3a0293ee, v75
	v_and_b32_e32 v78, 64, v158
	v_max3_f32 v12, v12, v74, v75
	v_fmamk_f32 v76, v92, 0x3a0293ee, v76
	v_fmac_f32_e32 v77, 0x3a0293ee, v93
	s_waitcnt lgkmcnt(0)
	v_fmac_f32_e32 v89, 0x3a0293ee, v73
	v_xor_b32_e32 v73, 16, v158
	v_add_u32_e32 v78, 64, v78
	v_max3_f32 v12, v12, v76, v77
	v_fmamk_f32 v70, v70, 0x3a0293ee, v86
	v_fmamk_f32 v71, v71, 0x3a0293ee, v87
	v_cmp_lt_i32_e32 vcc, v73, v78
	v_max3_f32 v12, v12, v70, v71
	v_fmamk_f32 v72, v72, 0x3a0293ee, v88
	v_cndmask_b32_e32 v73, v158, v73, vcc
	v_max3_f32 v12, v12, v72, v89
	v_lshlrev_b32_e32 v73, 2, v73
	v_mov_b32_e32 v84, v12
	s_nop 1
	v_permlane16_swap_b32_e32 v84, v12
	s_waitcnt lgkmcnt(0)
	v_max_f32_e32 v84, v84, v84
	v_max_f32_e32 v12, v12, v84
	v_xor_b32_e32 v84, 32, v158
	v_cmp_lt_i32_e32 vcc, v84, v78
	s_nop 1
	v_cndmask_b32_e32 v78, v158, v84, vcc
	v_lshlrev_b32_e32 v180, 2, v78
	v_mov_b32_e32 v78, v12
	s_nop 1
	v_permlane32_swap_b32_e32 v78, v12
	s_andn2_b64 vcc, exec, s[68:69]
	s_waitcnt lgkmcnt(0)
	v_max_f32_e32 v78, v78, v78
	v_max_f32_e32 v78, v12, v78
	v_sub_f32_e32 v2, v2, v78
	v_exp_f32_e32 v2, v2
	v_sub_f32_e32 v3, v3, v78
	v_exp_f32_e32 v3, v3
	v_sub_f32_e32 v4, v4, v78
	v_exp_f32_e32 v4, v4
	v_sub_f32_e32 v5, v5, v78
	v_exp_f32_e32 v5, v5
	v_sub_f32_e32 v6, v6, v78
	v_add_f32_e32 v12, 0, v2
	v_exp_f32_e32 v6, v6
	v_sub_f32_e32 v7, v7, v78
	v_add_f32_e32 v12, v3, v12
	v_exp_f32_e32 v7, v7
	v_sub_f32_e32 v8, v8, v78
	v_add_f32_e32 v12, v4, v12
	v_exp_f32_e32 v8, v8
	v_sub_f32_e32 v9, v9, v78
	v_add_f32_e32 v12, v5, v12
	v_exp_f32_e32 v9, v9
	v_sub_f32_e32 v13, v13, v78
	v_add_f32_e32 v12, v6, v12
	v_exp_f32_e32 v172, v13
	v_sub_f32_e32 v13, v54, v78
	v_add_f32_e32 v12, v7, v12
	v_exp_f32_e32 v173, v13
	v_sub_f32_e32 v13, v55, v78
	v_add_f32_e32 v12, v8, v12
	v_exp_f32_e32 v174, v13
	v_sub_f32_e32 v13, v57, v78
	v_add_f32_e32 v12, v9, v12
	v_exp_f32_e32 v175, v13
	v_sub_f32_e32 v13, v56, v78
	v_add_f32_e32 v12, v172, v12
	v_exp_f32_e32 v176, v13
	v_sub_f32_e32 v13, v66, v78
	v_add_f32_e32 v12, v173, v12
	v_exp_f32_e32 v177, v13
	v_sub_f32_e32 v13, v67, v78
	v_add_f32_e32 v12, v174, v12
	v_exp_f32_e32 v178, v13
	v_sub_f32_e32 v13, v69, v78
	v_add_f32_e32 v12, v175, v12
	v_exp_f32_e32 v179, v13
	v_sub_f32_e32 v13, v58, v78
	v_add_f32_e32 v12, v176, v12
	v_exp_f32_e32 v164, v13
	v_sub_f32_e32 v13, v59, v78
	v_add_f32_e32 v12, v177, v12
	v_exp_f32_e32 v165, v13
	v_sub_f32_e32 v13, v60, v78
	v_add_f32_e32 v12, v178, v12
	v_exp_f32_e32 v166, v13
	v_sub_f32_e32 v13, v61, v78
	v_add_f32_e32 v12, v179, v12
	v_exp_f32_e32 v167, v13
	v_sub_f32_e32 v13, v68, v78
	v_add_f32_e32 v12, v164, v12
	v_exp_f32_e32 v168, v13
	v_sub_f32_e32 v13, v79, v78
	v_add_f32_e32 v12, v165, v12
	v_exp_f32_e32 v169, v13
	v_sub_f32_e32 v13, v80, v78
	v_add_f32_e32 v12, v166, v12
	v_exp_f32_e32 v170, v13
	v_sub_f32_e32 v13, v81, v78
	v_add_f32_e32 v12, v167, v12
	v_exp_f32_e32 v171, v13
	v_sub_f32_e32 v13, v62, v78
	v_add_f32_e32 v12, v168, v12
	v_exp_f32_e32 v88, v13
	v_sub_f32_e32 v13, v63, v78
	v_add_f32_e32 v12, v169, v12
	v_exp_f32_e32 v90, v13
	v_sub_f32_e32 v13, v64, v78
	v_add_f32_e32 v12, v170, v12
	v_exp_f32_e32 v91, v13
	v_sub_f32_e32 v13, v65, v78
	v_add_f32_e32 v12, v171, v12
	v_exp_f32_e32 v92, v13
	v_sub_f32_e32 v10, v10, v78
	v_add_f32_e32 v12, v88, v12
	v_exp_f32_e32 v93, v10
	v_add_f32_e32 v12, v90, v12
	v_add_f32_e32 v12, v91, v12
	v_add_f32_e32 v12, v92, v12
	v_add_f32_e32 v10, v93, v12
	v_sub_f32_e32 v12, v82, v78
	v_exp_f32_e32 v161, v12
	v_sub_f32_e32 v12, v83, v78
	v_exp_f32_e32 v162, v12
	v_sub_f32_e32 v12, v85, v78
	v_exp_f32_e32 v163, v12
	v_sub_f32_e32 v12, v74, v78
	v_exp_f32_e32 v81, v12
	v_sub_f32_e32 v12, v75, v78
	v_add_f32_e32 v10, v161, v10
	v_exp_f32_e32 v82, v12
	v_sub_f32_e32 v12, v76, v78
	v_add_f32_e32 v10, v162, v10
	v_exp_f32_e32 v83, v12
	v_sub_f32_e32 v12, v77, v78
	v_add_f32_e32 v10, v163, v10
	v_exp_f32_e32 v84, v12
	v_sub_f32_e32 v12, v70, v78
	v_add_f32_e32 v10, v81, v10
	v_exp_f32_e32 v85, v12
	v_sub_f32_e32 v12, v71, v78
	v_add_f32_e32 v10, v82, v10
	v_exp_f32_e32 v86, v12
	v_sub_f32_e32 v12, v72, v78
	v_add_f32_e32 v10, v83, v10
	v_exp_f32_e32 v87, v12
	v_sub_f32_e32 v12, v89, v78
	v_add_f32_e32 v10, v84, v10
	v_exp_f32_e32 v89, v12
	v_add_f32_e32 v10, v85, v10
	v_add_f32_e32 v10, v86, v10
	v_add_f32_e32 v10, v87, v10
	v_add_f32_e32 v10, v89, v10
	v_mov_b32_e32 v12, v10
	s_nop 1
	v_permlane16_swap_b32_e32 v12, v10
	s_waitcnt lgkmcnt(0)
	v_add_f32_e32 v79, v10, v12
	v_mov_b32_e32 v80, v79
	s_nop 1
	v_permlane32_swap_b32_e32 v80, v79
	s_cbranch_vccnz .LBB0_391
	s_and_b64 s[16:17], s[46:47], exec
	s_cselect_b32 s16, s43, s86
	v_add_u32_e32 v10, s16, v157
	v_cvt_pk_bf16_f32 v54, v2, v3
	v_cvt_pk_bf16_f32 v55, v4, v5
	v_cvt_pk_bf16_f32 v56, v6, v7
	v_cvt_pk_bf16_f32 v57, v8, v9
	v_add_u32_e32 v4, v10, v149
	v_add_u32_e32 v8, v10, v150
	v_add_u32_e32 v12, v10, v151
	ds_read_b64_tr_b16 v[2:3], v4
	ds_read_b64_tr_b16 v[4:5], v4 offset:4096
	ds_read_b64_tr_b16 v[6:7], v8
	ds_read_b64_tr_b16 v[8:9], v8 offset:4096
	ds_read_b64_tr_b16 v[58:59], v12
	ds_read_b64_tr_b16 v[60:61], v12 offset:4096
	v_add_u32_e32 v12, v10, v152
	ds_read_b64_tr_b16 v[62:63], v12
	ds_read_b64_tr_b16 v[64:65], v12 offset:4096
	v_add_u32_e32 v12, v10, v153
	ds_read_b64_tr_b16 v[66:67], v12
	ds_read_b64_tr_b16 v[68:69], v12 offset:4096
	v_add_u32_e32 v12, v10, v154
	ds_read_b64_tr_b16 v[70:71], v12
	ds_read_b64_tr_b16 v[72:73], v12 offset:4096
	v_add_u32_e32 v12, v10, v155
	v_add_u32_e32 v10, v10, v156
	ds_read_b64_tr_b16 v[180:181], v12
	ds_read_b64_tr_b16 v[182:183], v12 offset:4096
	ds_read_b64_tr_b16 v[184:185], v10
	ds_read_b64_tr_b16 v[186:187], v10 offset:4096
	s_waitcnt lgkmcnt(14)
	v_mfma_f32_16x16x32_bf16 v[2:5], v[2:5], v[54:57], 0
	s_waitcnt lgkmcnt(12)
	v_mfma_f32_16x16x32_bf16 v[6:9], v[6:9], v[54:57], 0
	s_waitcnt lgkmcnt(10)
	v_mfma_f32_16x16x32_bf16 v[58:61], v[58:61], v[54:57], 0
	s_waitcnt lgkmcnt(8)
	v_mfma_f32_16x16x32_bf16 v[62:65], v[62:65], v[54:57], 0
	s_waitcnt lgkmcnt(6)
	v_mfma_f32_16x16x32_bf16 v[66:69], v[66:69], v[54:57], 0
	s_waitcnt lgkmcnt(4)
	v_mfma_f32_16x16x32_bf16 v[74:77], v[70:73], v[54:57], 0
	s_waitcnt lgkmcnt(2)
	v_mfma_f32_16x16x32_bf16 v[70:73], v[180:183], v[54:57], 0
	s_waitcnt lgkmcnt(0)
	v_mfma_f32_16x16x32_bf16 v[54:57], v[184:187], v[54:57], 0
	s_branch .LBB0_392
